# GEMM K-loops: wave-uniform relaxed-wait test taken directly from the scalar mask (no VALU/readfirstlane chain); stick-breaking masked path: compare-to-select pairs padded to the 2 wait states the ISA
# speedup vs baseline: 1.0162x; 1.0039x over previous
; #define PG8_STAGEA(bufoff, h, ap, kb, go) do { if constexpr (GATHER) { PG8_STAGE(bufoff, (const char*)g.A + (kb), go[h]); } else { PG8_STAGE(bufoff, (ap) + (h) * hstep, voffA); } } while (0)
; #define PG8_WAIT_L(n) asm volatile("s_waitcnt lgkmcnt(" #n ")" ::: "memory")
; #define PG8_WAIT_V8R() do { if (relax) { if (GATHER && wid == 0 && has_next) asm volatile("s_waitcnt vmcnt(%0)" :: "n"(9 + Epi::NSTORES) : "memory"); else asm volatile("s_waitcnt vmcnt(%0)" :: "n"(8 + Epi::NSTORES) : "memory"); } else PG8_WAIT_V(8); } while (0)
; #define PG8_BAR __builtin_amdgcn_s_barrier()
; #define PG8_SCHED __builtin_amdgcn_sched_barrier(0)
; template <class Epi, class Sched, bool GATHER, bool FP8 = false>
; __device__ __forceinline__ void gemm_phase(LAS unsigned char* lds, LAS int* idx, const Gemm g, const Sched& S, const Epi& E) {
;     ...
;             const int relax = __builtin_amdgcn_readfirstlane(((t == 0) && (ui > 0)) ? 1 : 0);
;             PG8_LDB(B0, 0, 0); PG8_LDB(B1, 0, 1); PG8_SCHED; PG8_LDA(At, 0, 0); PG8_STAGEA(PG8_SA(1, 1), 1, a1, k1, gc);
;             PG8_WAIT_V8R(); PG8_WAIT_L(0); PG8_BAR; PG8_MMA(0, 0, At, B0); PG8_MMA(0, 1, At, B1); PG8_BAR; PG8_SCHED;
.LBB0_289:
	ds_read_b128 v[26:29], v226
	ds_read_b128 v[30:33], v227
	ds_read_b128 v[18:21], v228
	ds_read_b128 v[22:25], v229
	ds_read_b128 v[10:13], v231
	ds_read_b128 v[14:17], v232
	ds_read_b128 v[2:5], v233
	ds_read_b128 v[6:9], v234
	s_cmp_eq_u32 s66, 0
	s_cselect_b64 s[30:31], -1, 0
	s_and_b64 s[30:31], s[26:27], s[30:31]
	v_lshl_add_u64 v[214:215], v[210:211], 0, s[28:29]
	s_add_i32 m0, s43, 0xc000
	ds_read_b128 v[58:61], v244
	ds_read_b128 v[62:65], v244 offset:1024
	ds_read_b128 v[50:53], v244 offset:2048
	ds_read_b128 v[54:57], v244 offset:3072
	ds_read_b128 v[42:45], v244 offset:4096
	ds_read_b128 v[46:49], v244 offset:5120
	ds_read_b128 v[34:37], v244 offset:6144
	ds_read_b128 v[38:41], v244 offset:7168
	global_load_lds_dwordx4 v[214:215], off
	v_lshl_add_u64 v[214:215], v[212:213], 0, s[28:29]
	s_add_i32 m0, s43, 0xe000
	s_nop 0
	global_load_lds_dwordx4 v[214:215], off
	s_and_b64 vcc, exec, s[30:31]
	s_not_b64 s[34:35], s[30:31]
	s_mov_b64 s[30:31], -1
	s_cbranch_vccnz .LBB0_291
	s_waitcnt vmcnt(8)
	s_mov_b64 s[30:31], 0

; #define LAS __attribute__((address_space(3)))
; __device__ __forceinline__ int crow(int r, int hi) { return (r & 3) + 8 * (r >> 2) + 4 * hi; }
; __device__ __forceinline__ void qkt(f32x16& p0, f32x16& p1, const LAS char* Ks, const bf16x8* qr, int r32, int hi) {
;     p0 = f32x16{}; p1 = f32x16{};
; #pragma unroll
;     for (int d0 = 0; d0 < 8; ++d0) { const int cb = (d0 * 16 + hi * 8) * 2;
;         const bf16x8 b0 = *(const LAS bf16x8*)(Ks + KSWZ(r32, cb));
;         const bf16x8 b1 = *(const LAS bf16x8*)(Ks + KSWZ(32 + r32, cb));
;         p0 = __builtin_amdgcn_mfma_f32_32x32x16_bf16(b0, qr[d0], p0, 0, 0, 0);
;         p1 = __builtin_amdgcn_mfma_f32_32x32x16_bf16(b1, qr[d0], p1, 0, 0, 0); }
; template <int MODE>
; __device__ __forceinline__ void attn_unit(const AttnArgs& A, int b, int qb, int qc, int kc, int vc, int oc, float slope2, int dmax, LAS char* lds) {
;     ...
;             qkt(p0, p1, lds + L_K + bf * SHM_T, qr, r32, hi);
;             const int vb = vb0 + bf * SHM_T;
;             bf16x8 pa0, pa1, pa2, pa3;
;             if (MODE == 0) {
;                 const bool need_mask = (k0 + 63 >= r0);
;                 float lsum = 0.f;
;                 float lk0[16], lk1[16];
; #pragma unroll
;                 for (int r = 0; r < 16; ++r) {
;                     { const float zl = p0[r] * QK_C, u = __builtin_amdgcn_exp2f(-fabsf(zl)), L = __builtin_amdgcn_logf(1.f + u), sp = fmaxf(zl, 0.f) + L;
;                       const bool ok = !need_mask || (k0 + crow(r, hi) < tq); lk0[r] = ok ? -sp : 0.f; p0[r] = ok ? (zl - sp) : -INFINITY; lsum += lk0[r]; }
;                     { const float zl = p1[r] * QK_C, u = __builtin_amdgcn_exp2f(-fabsf(zl)), L = __builtin_amdgcn_logf(1.f + u), sp = fmaxf(zl, 0.f) + L;
;                       const bool ok = !need_mask || (k0 + 32 + crow(r, hi) < tq); lk1[r] = ok ? -sp : 0.f; p1[r] = ok ? (zl - sp) : -INFINITY; lsum += lk1[r]; }
.LBB0_372:
	s_cmp_gt_i32 s38, s35
	s_cselect_b64 s[16:17], -1, 0
	s_or_b64 s[16:17], s[16:17], s[14:15]
	s_and_b64 vcc, exec, s[16:17]
	s_cbranch_vccnz .LBB0_374
	s_lshl_b32 s16, s41, 14
	v_add_u32_e32 v67, s16, v199
	v_add_u32_e32 v72, v67, v184
	ds_read_b128 v[68:71], v72 offset:32768
	ds_read_b128 v[72:75], v72 offset:40960
	v_add_u32_e32 v104, v67, v185
	ds_read_b128 v[100:103], v104 offset:32768
	ds_read_b128 v[104:107], v104 offset:40960
	s_add_i32 s14, s38, 63
	s_waitcnt lgkmcnt(0)
	v_mfma_f32_32x32x16_bf16 v[84:99], v[68:71], v[122:125], 0
	s_cmp_lt_i32 s14, s35
	s_cselect_b64 s[14:15], -1, 0
	v_mov_b32_e32 v254, 0x7fffffff
	v_cndmask_b32_e64 v253, v210, v254, s[14:15]
	s_mov_b32 s22, s20
	s_mov_b32 s23, s20
	s_mov_b32 s21, s20
	v_mfma_f32_32x32x16_bf16 v[68:83], v[72:75], v[122:125], 0
	v_mfma_f32_32x32x16_bf16 v[84:99], v[100:103], v[126:129], v[84:99]
	v_mfma_f32_32x32x16_bf16 v[68:83], v[104:107], v[126:129], v[68:83]
	v_add_u32_e32 v104, v67, v186
	ds_read_b128 v[100:103], v104 offset:32768
	ds_read_b128 v[104:107], v104 offset:40960
	s_waitcnt lgkmcnt(0)
	v_mfma_f32_32x32x16_bf16 v[84:99], v[100:103], v[130:133], v[84:99]
	v_mfma_f32_32x32x16_bf16 v[68:83], v[104:107], v[130:133], v[68:83]
	v_add_u32_e32 v104, v67, v187
	ds_read_b128 v[100:103], v104 offset:32768
	ds_read_b128 v[104:107], v104 offset:40960
	s_waitcnt lgkmcnt(0)
	v_mfma_f32_32x32x16_bf16 v[84:99], v[100:103], v[134:137], v[84:99]
	v_mfma_f32_32x32x16_bf16 v[68:83], v[104:107], v[134:137], v[68:83]
	v_add_u32_e32 v104, v67, v188
	ds_read_b128 v[100:103], v104 offset:32768
	ds_read_b128 v[104:107], v104 offset:40960
	s_waitcnt lgkmcnt(0)
	v_mfma_f32_32x32x16_bf16 v[84:99], v[100:103], v[138:141], v[84:99]
	v_mfma_f32_32x32x16_bf16 v[68:83], v[104:107], v[138:141], v[68:83]
	v_add_u32_e32 v104, v67, v189
	ds_read_b128 v[100:103], v104 offset:32768
	ds_read_b128 v[104:107], v104 offset:40960
	s_waitcnt lgkmcnt(0)
	v_mfma_f32_32x32x16_bf16 v[84:99], v[100:103], v[142:145], v[84:99]
	v_mfma_f32_32x32x16_bf16 v[68:83], v[104:107], v[142:145], v[68:83]
	v_add_u32_e32 v104, v67, v190
	ds_read_b128 v[100:103], v104 offset:32768
	ds_read_b128 v[104:107], v104 offset:40960
	v_add_u32_e32 v67, v67, v191
	s_waitcnt lgkmcnt(0)
	v_mfma_f32_32x32x16_bf16 v[84:99], v[100:103], v[146:149], v[84:99]
	v_mfma_f32_32x32x16_bf16 v[68:83], v[104:107], v[146:149], v[68:83]
	ds_read_b128 v[100:103], v67 offset:32768
	ds_read_b128 v[104:107], v67 offset:40960
	v_add_u32_e32 v67, s38, v192
	v_sub_u32_e32 v254, v253, v67
	v_cmp_lt_i32_e32 vcc, 0, v254
	s_waitcnt lgkmcnt(0)
	v_mfma_f32_32x32x16_bf16 v[84:99], v[100:103], v[150:153], v[84:99]
	v_mfma_f32_32x32x16_bf16 v[68:83], v[104:107], v[150:153], v[68:83]
	s_nop 9
	s_cmp_lg_u64 s[14:15], 0
	s_cbranch_scc1 .Lsb_unmasked
	v_mul_f32_e32 v100, 0x3e0293ee, v84
	v_exp_f32_e64 v102, -|v100|
	v_max_f32_e32 v100, 0, v100
	v_add_f32_e32 v102, 1.0, v102
	v_log_f32_e32 v102, v102
	s_nop 0
	v_add_f32_e32 v102, v100, v102
	v_fma_f32 v84, v84, s26, -v102
	v_cndmask_b32_e32 v211, v208, v84, vcc
	v_mul_f32_e32 v84, 0x3e0293ee, v68
	v_exp_f32_e64 v103, -|v84|
	v_max_f32_e32 v84, 0, v84
	v_cndmask_b32_e64 v100, 0, -v102, vcc
	v_cmp_lt_i32_e32 vcc, 32, v254
	v_add_f32_e32 v103, 1.0, v103
	v_log_f32_e32 v103, v103
	v_add_f32_e32 v102, 0, v100
	v_add_f32_e32 v103, v84, v103
	v_fma_f32 v68, v68, s26, -v103
	v_cndmask_b32_e64 v84, 0, -v103, vcc
	v_cndmask_b32_e32 v212, v208, v68, vcc
	v_mul_f32_e32 v68, 0x3e0293ee, v85
	v_add_f32_e32 v101, v102, v84
	v_exp_f32_e64 v102, -|v68|
	v_max_f32_e32 v68, 0, v68
	v_add_f32_e32 v102, 1.0, v102
	v_log_f32_e32 v102, v102
	s_nop 0
	v_add_f32_e32 v102, v68, v102
	v_cmp_lt_i32_e32 vcc, 1, v254
	v_fma_f32 v85, v85, s26, -v102
	s_nop 0
	v_cndmask_b32_e32 v213, v208, v85, vcc
	v_mul_f32_e32 v85, 0x3e0293ee, v69
	v_cndmask_b32_e64 v68, 0, -v102, vcc
	v_exp_f32_e64 v102, -|v85|
	v_max_f32_e32 v85, 0, v85
	v_add_f32_e32 v101, v68, v101
	v_add_f32_e32 v102, 1.0, v102
	v_log_f32_e32 v102, v102
	s_nop 0
	v_add_f32_e32 v102, v85, v102
	v_cmp_lt_i32_e32 vcc, 33, v254
	v_fma_f32 v69, v69, s26, -v102
	s_nop 0
	v_cndmask_b32_e32 v214, v208, v69, vcc
	v_mul_f32_e32 v69, 0x3e0293ee, v86
	v_cndmask_b32_e64 v85, 0, -v102, vcc
	v_exp_f32_e64 v102, -|v69|
	v_max_f32_e32 v69, 0, v69
	v_add_f32_e32 v101, v85, v101
	v_cvt_pkrtz_f16_f32 v238, v84, v85
	v_add_f32_e32 v102, 1.0, v102
	v_log_f32_e32 v102, v102
	s_nop 0
	v_add_f32_e32 v102, v69, v102
	v_cmp_lt_i32_e32 vcc, 2, v254
	v_fma_f32 v86, v86, s26, -v102
	s_nop 0
	v_cndmask_b32_e32 v215, v208, v86, vcc
	v_mul_f32_e32 v86, 0x3e0293ee, v70
	v_cndmask_b32_e64 v69, 0, -v102, vcc
	v_exp_f32_e64 v102, -|v86|
	v_max_f32_e32 v86, 0, v86
	v_add_f32_e32 v101, v69, v101
	v_add_f32_e32 v102, 1.0, v102
	v_log_f32_e32 v102, v102
	s_nop 0
	v_add_f32_e32 v102, v86, v102
	v_cmp_lt_i32_e32 vcc, 34, v254
	v_fma_f32 v70, v70, s26, -v102
	s_nop 0
	v_cndmask_b32_e32 v216, v208, v70, vcc
	v_mul_f32_e32 v70, 0x3e0293ee, v87
	v_cndmask_b32_e64 v86, 0, -v102, vcc
	v_exp_f32_e64 v102, -|v70|
	v_max_f32_e32 v70, 0, v70
	v_add_f32_e32 v101, v86, v101
	v_add_f32_e32 v102, 1.0, v102
	v_log_f32_e32 v102, v102
	s_nop 0
	v_add_f32_e32 v102, v70, v102
	v_cmp_lt_i32_e32 vcc, 3, v254
	v_fma_f32 v87, v87, s26, -v102
	s_nop 0
	v_cndmask_b32_e32 v217, v208, v87, vcc
	v_mul_f32_e32 v87, 0x3e0293ee, v71
	v_cndmask_b32_e64 v70, 0, -v102, vcc
	v_exp_f32_e64 v102, -|v87|
	v_max_f32_e32 v87, 0, v87
	v_add_f32_e32 v101, v70, v101
	v_add_f32_e32 v102, 1.0, v102
	v_log_f32_e32 v102, v102
	s_nop 0
	v_add_f32_e32 v102, v87, v102
	v_cmp_lt_i32_e32 vcc, 35, v254
	v_fma_f32 v71, v71, s26, -v102
	s_nop 0
	v_cndmask_b32_e32 v218, v208, v71, vcc
; __device__ __forceinline__ int crow(int r, int hi) { return (r & 3) + 8 * (r >> 2) + 4 * hi; }
; template <int MODE>
; __device__ __forceinline__ void attn_unit(const AttnArgs& A, int b, int qb, int qc, int kc, int vc, int oc, float slope2, int dmax, LAS char* lds) {
;     ...
;                 for (int r = 0; r < 16; ++r) {
;                     { const float zl = p0[r] * QK_C, u = __builtin_amdgcn_exp2f(-fabsf(zl)), L = __builtin_amdgcn_logf(1.f + u), sp = fmaxf(zl, 0.f) + L;
;                       const bool ok = !need_mask || (k0 + crow(r, hi) < tq); lk0[r] = ok ? -sp : 0.f; p0[r] = ok ? (zl - sp) : -INFINITY; lsum += lk0[r]; }
;                     { const float zl = p1[r] * QK_C, u = __builtin_amdgcn_exp2f(-fabsf(zl)), L = __builtin_amdgcn_logf(1.f + u), sp = fmaxf(zl, 0.f) + L;
;                       const bool ok = !need_mask || (k0 + 32 + crow(r, hi) < tq); lk1[r] = ok ? -sp : 0.f; p1[r] = ok ? (zl - sp) : -INFINITY; lsum += lk1[r]; }
;                 }
;                 f16x8 f0, f1, f2, f3; PK4H(lk0, 0, f0); PK4H(lk0, 8, f1); PK4H(lk1, 0, f2); PK4H(lk1, 8, f3);
	v_mul_f32_e32 v71, 0x3e0293ee, v88
	v_cndmask_b32_e64 v87, 0, -v102, vcc
	v_exp_f32_e64 v102, -|v71|
	v_max_f32_e32 v71, 0, v71
	v_add_f32_e32 v101, v87, v101
	v_cvt_pkrtz_f16_f32 v239, v86, v87
	v_add_f32_e32 v102, 1.0, v102
	v_log_f32_e32 v102, v102
	s_nop 0
	v_add_f32_e32 v102, v71, v102
	v_cmp_lt_i32_e32 vcc, 8, v254
	v_fma_f32 v88, v88, s26, -v102
	s_nop 0
	v_cndmask_b32_e32 v219, v208, v88, vcc
	v_mul_f32_e32 v88, 0x3e0293ee, v72
	v_cndmask_b32_e64 v71, 0, -v102, vcc
	v_exp_f32_e64 v102, -|v88|
	v_max_f32_e32 v88, 0, v88
	v_add_f32_e32 v101, v71, v101
	v_add_f32_e32 v102, 1.0, v102
	v_log_f32_e32 v102, v102
	s_nop 0
	v_add_f32_e32 v102, v88, v102
	v_cmp_lt_i32_e32 vcc, 40, v254
	v_fma_f32 v72, v72, s26, -v102
	s_nop 0
	v_cndmask_b32_e32 v220, v208, v72, vcc
	v_mul_f32_e32 v72, 0x3e0293ee, v89
	v_cndmask_b32_e64 v88, 0, -v102, vcc
	v_exp_f32_e64 v102, -|v72|
	v_max_f32_e32 v72, 0, v72
	v_add_f32_e32 v101, v88, v101
	v_add_f32_e32 v102, 1.0, v102
	v_log_f32_e32 v102, v102
	s_nop 0
	v_add_f32_e32 v102, v72, v102
	v_cmp_lt_i32_e32 vcc, 9, v254
	v_fma_f32 v89, v89, s26, -v102
	s_nop 0
	v_cndmask_b32_e32 v221, v208, v89, vcc
	v_mul_f32_e32 v89, 0x3e0293ee, v73
	v_cndmask_b32_e64 v72, 0, -v102, vcc
	v_exp_f32_e64 v102, -|v89|
	v_max_f32_e32 v89, 0, v89
	v_add_f32_e32 v101, v72, v101
	v_add_f32_e32 v102, 1.0, v102
	v_log_f32_e32 v102, v102
	s_nop 0
	v_add_f32_e32 v102, v89, v102
	v_cmp_lt_i32_e32 vcc, 41, v254
	v_fma_f32 v73, v73, s26, -v102
	s_nop 0
	v_cndmask_b32_e32 v222, v208, v73, vcc
	v_mul_f32_e32 v73, 0x3e0293ee, v90
	v_cndmask_b32_e64 v89, 0, -v102, vcc
	v_exp_f32_e64 v102, -|v73|
	v_max_f32_e32 v73, 0, v73
	v_add_f32_e32 v101, v89, v101
	v_cvt_pkrtz_f16_f32 v240, v88, v89
	v_add_f32_e32 v102, 1.0, v102
	v_log_f32_e32 v102, v102
	v_permlane32_swap_b32_e32 v238, v240
	v_add_f32_e32 v102, v73, v102
	v_cmp_lt_i32_e32 vcc, 10, v254
	v_fma_f32 v90, v90, s26, -v102
	s_nop 0
	v_cndmask_b32_e32 v223, v208, v90, vcc
	v_mul_f32_e32 v90, 0x3e0293ee, v74
	v_cndmask_b32_e64 v73, 0, -v102, vcc
	v_exp_f32_e64 v102, -|v90|
	v_max_f32_e32 v90, 0, v90
	v_add_f32_e32 v101, v73, v101
	v_add_f32_e32 v102, 1.0, v102
	v_log_f32_e32 v102, v102
	s_nop 0
	v_add_f32_e32 v102, v90, v102
	v_cmp_lt_i32_e32 vcc, 42, v254
	v_fma_f32 v74, v74, s26, -v102
	s_nop 0
	v_cndmask_b32_e32 v224, v208, v74, vcc
	v_mul_f32_e32 v74, 0x3e0293ee, v91
	v_cndmask_b32_e64 v90, 0, -v102, vcc
	v_exp_f32_e64 v102, -|v74|
	v_max_f32_e32 v74, 0, v74
	v_add_f32_e32 v101, v90, v101
	v_add_f32_e32 v102, 1.0, v102
	v_log_f32_e32 v102, v102
	s_nop 0
	v_add_f32_e32 v102, v74, v102
	v_cmp_lt_i32_e32 vcc, 11, v254
	v_fma_f32 v91, v91, s26, -v102
	s_nop 0
	v_cndmask_b32_e32 v225, v208, v91, vcc
	v_mul_f32_e32 v91, 0x3e0293ee, v75
	v_cndmask_b32_e64 v74, 0, -v102, vcc
	v_exp_f32_e64 v102, -|v91|
	v_max_f32_e32 v91, 0, v91
	v_add_f32_e32 v101, v74, v101
	v_add_f32_e32 v102, 1.0, v102
	v_log_f32_e32 v102, v102
	s_nop 0
	v_add_f32_e32 v102, v91, v102
	v_cmp_lt_i32_e32 vcc, 43, v254
	v_fma_f32 v75, v75, s26, -v102
	s_nop 0
	v_cndmask_b32_e32 v226, v208, v75, vcc
	v_mul_f32_e32 v75, 0x3e0293ee, v92
	v_cndmask_b32_e64 v91, 0, -v102, vcc
	v_exp_f32_e64 v102, -|v75|
	v_max_f32_e32 v75, 0, v75
	v_add_f32_e32 v101, v91, v101
	v_cvt_pkrtz_f16_f32 v241, v90, v91
	v_add_f32_e32 v102, 1.0, v102
	v_log_f32_e32 v102, v102
	v_permlane32_swap_b32_e32 v239, v241
	v_add_f32_e32 v102, v75, v102
	v_cmp_lt_i32_e32 vcc, 16, v254
	v_fma_f32 v92, v92, s26, -v102
	s_nop 0
	v_cndmask_b32_e32 v227, v208, v92, vcc
	v_mul_f32_e32 v92, 0x3e0293ee, v76
	v_cndmask_b32_e64 v75, 0, -v102, vcc
	v_exp_f32_e64 v102, -|v92|
	v_max_f32_e32 v92, 0, v92
	v_add_f32_e32 v101, v75, v101
	v_add_f32_e32 v102, 1.0, v102
	v_log_f32_e32 v102, v102
	s_nop 0
	v_add_f32_e32 v102, v92, v102
	v_cmp_lt_i32_e32 vcc, 48, v254
	v_fma_f32 v76, v76, s26, -v102
	s_nop 0
	v_cndmask_b32_e32 v228, v208, v76, vcc
	v_mul_f32_e32 v76, 0x3e0293ee, v93
	v_cndmask_b32_e64 v92, 0, -v102, vcc
	v_exp_f32_e64 v102, -|v76|
	v_max_f32_e32 v76, 0, v76
	v_add_f32_e32 v101, v92, v101
	v_add_f32_e32 v102, 1.0, v102
	v_log_f32_e32 v102, v102
	s_nop 0
	v_add_f32_e32 v102, v76, v102
	v_cmp_lt_i32_e32 vcc, 17, v254
	v_fma_f32 v93, v93, s26, -v102
	s_nop 0
	v_cndmask_b32_e32 v229, v208, v93, vcc
	v_mul_f32_e32 v93, 0x3e0293ee, v77
	v_cndmask_b32_e64 v76, 0, -v102, vcc
	v_exp_f32_e64 v102, -|v93|
	v_max_f32_e32 v93, 0, v93
	v_add_f32_e32 v101, v76, v101
	v_add_f32_e32 v102, 1.0, v102
	v_log_f32_e32 v102, v102
	s_nop 0
	v_add_f32_e32 v102, v93, v102
	v_cmp_lt_i32_e32 vcc, 49, v254
	v_fma_f32 v77, v77, s26, -v102
	s_nop 0
	v_cndmask_b32_e32 v231, v208, v77, vcc
	v_mul_f32_e32 v77, 0x3e0293ee, v94
	v_cndmask_b32_e64 v93, 0, -v102, vcc
	v_exp_f32_e64 v102, -|v77|
	v_max_f32_e32 v77, 0, v77
	v_add_f32_e32 v101, v93, v101
	v_cvt_pkrtz_f16_f32 v242, v92, v93
	v_add_f32_e32 v102, 1.0, v102
	v_log_f32_e32 v102, v102
	s_nop 0
	v_add_f32_e32 v102, v77, v102
	v_cmp_lt_i32_e32 vcc, 18, v254
	v_fma_f32 v94, v94, s26, -v102
	s_nop 0
	v_cndmask_b32_e64 v77, 0, -v102, vcc
; __device__ __forceinline__ int crow(int r, int hi) { return (r & 3) + 8 * (r >> 2) + 4 * hi; }
; template <int MODE>
; __device__ __forceinline__ void attn_unit(const AttnArgs& A, int b, int qb, int qc, int kc, int vc, int oc, float slope2, int dmax, LAS char* lds) {
;     ...
;                 for (int r = 0; r < 16; ++r) {
;                     { const float zl = p0[r] * QK_C, u = __builtin_amdgcn_exp2f(-fabsf(zl)), L = __builtin_amdgcn_logf(1.f + u), sp = fmaxf(zl, 0.f) + L;
;                       const bool ok = !need_mask || (k0 + crow(r, hi) < tq); lk0[r] = ok ? -sp : 0.f; p0[r] = ok ? (zl - sp) : -INFINITY; lsum += lk0[r]; }
;                     { const float zl = p1[r] * QK_C, u = __builtin_amdgcn_exp2f(-fabsf(zl)), L = __builtin_amdgcn_logf(1.f + u), sp = fmaxf(zl, 0.f) + L;
;                       const bool ok = !need_mask || (k0 + 32 + crow(r, hi) < tq); lk1[r] = ok ? -sp : 0.f; p1[r] = ok ? (zl - sp) : -INFINITY; lsum += lk1[r]; }
;                 }
;                 f16x8 f0, f1, f2, f3; PK4H(lk0, 0, f0); PK4H(lk0, 8, f1); PK4H(lk1, 0, f2); PK4H(lk1, 8, f3);
;                 f32x16 w0, w1;
; #pragma unroll
;                 for (int r = 0; r < 16; ++r) { w0[r] = carry; w1[r] = carry; }
	v_cndmask_b32_e32 v232, v208, v94, vcc
	v_add_f32_e32 v94, v77, v101
	v_mul_f32_e32 v101, 0x3e0293ee, v78
	v_exp_f32_e64 v102, -|v101|
	v_max_f32_e32 v101, 0, v101
	v_add_f32_e32 v102, 1.0, v102
	v_log_f32_e32 v102, v102
	s_nop 0
	v_add_f32_e32 v101, v101, v102
	v_cmp_lt_i32_e32 vcc, 50, v254
	v_fma_f32 v78, v78, s26, -v101
	s_nop 0
	v_cndmask_b32_e64 v106, 0, -v101, vcc
	v_cndmask_b32_e32 v233, v208, v78, vcc
	v_add_f32_e32 v78, v106, v94
	v_mul_f32_e32 v94, 0x3e0293ee, v95
	v_exp_f32_e64 v101, -|v94|
	v_max_f32_e32 v94, 0, v94
	v_cvt_pkrtz_f16_f32 v102, v75, v76
	v_mov_b32_e32 v75, v66
	v_add_f32_e32 v101, 1.0, v101
	v_log_f32_e32 v101, v101
	v_mov_b32_e32 v76, v66
	v_add_f32_e32 v94, v94, v101
	v_cmp_lt_i32_e32 vcc, 19, v254
	v_cvt_pkrtz_f16_f32 v101, v73, v74
	s_nop 0
	v_cndmask_b32_e64 v103, 0, -v94, vcc
	v_fma_f32 v94, v95, s26, -v94
	v_cndmask_b32_e32 v234, v208, v94, vcc
	v_mul_f32_e32 v94, 0x3e0293ee, v79
	v_exp_f32_e64 v95, -|v94|
	v_max_f32_e32 v94, 0, v94
	v_add_f32_e32 v78, v103, v78
	v_cvt_pkrtz_f16_f32 v103, v77, v103
	v_add_f32_e32 v95, 1.0, v95
	v_log_f32_e32 v95, v95
	v_mov_b32_e32 v73, v66
	v_mov_b32_e32 v74, v66
	v_mov_b32_e32 v77, v66
	v_add_f32_e32 v94, v94, v95
	v_cmp_lt_i32_e32 vcc, 51, v254
	v_fma_f32 v79, v79, s26, -v94
	s_nop 0
	v_cndmask_b32_e32 v235, v208, v79, vcc
	v_mul_f32_e32 v79, 0x3e0293ee, v96
	v_cndmask_b32_e64 v95, 0, -v94, vcc
	v_exp_f32_e64 v94, -|v79|
	v_max_f32_e32 v79, 0, v79
	v_add_f32_e32 v78, v95, v78
	v_cvt_pkrtz_f16_f32 v243, v106, v95
	v_add_f32_e32 v94, 1.0, v94
	v_log_f32_e32 v94, v94
	s_nop 0
	v_add_f32_e32 v79, v79, v94
	v_cmp_lt_i32_e32 vcc, 24, v254
	s_nop 0
	s_nop 0
	v_cndmask_b32_e64 v94, 0, -v79, vcc
	v_fma_f32 v79, v96, s26, -v79
	v_cndmask_b32_e32 v236, v208, v79, vcc
	v_mul_f32_e32 v79, 0x3e0293ee, v80
	v_exp_f32_e64 v96, -|v79|
	v_max_f32_e32 v79, 0, v79
	v_add_f32_e32 v78, v94, v78
	v_add_f32_e32 v96, 1.0, v96
	v_log_f32_e32 v96, v96
	s_nop 0
	v_add_f32_e32 v79, v79, v96
	v_cmp_lt_i32_e32 vcc, 56, v254
	s_nop 0
	s_nop 0
	v_cndmask_b32_e64 v96, 0, -v79, vcc
	v_fma_f32 v79, v80, s26, -v79
	v_cndmask_b32_e32 v237, v208, v79, vcc
	v_mul_f32_e32 v79, 0x3e0293ee, v97
	v_exp_f32_e64 v80, -|v79|
	v_max_f32_e32 v79, 0, v79
	v_add_f32_e32 v78, v96, v78
	v_add_f32_e32 v80, 1.0, v80
	v_log_f32_e32 v80, v80
	s_nop 0
	v_add_f32_e32 v79, v79, v80
	v_cmp_lt_i32_e32 vcc, 25, v254
	s_nop 0
	s_nop 0
	v_cndmask_b32_e64 v80, 0, -v79, vcc
	v_fma_f32 v79, v97, s26, -v79
	v_cndmask_b32_e32 v246, v208, v79, vcc
	v_mul_f32_e32 v79, 0x3e0293ee, v81
	v_exp_f32_e64 v97, -|v79|
	v_max_f32_e32 v79, 0, v79
	v_add_f32_e32 v78, v80, v78
	v_cvt_pkrtz_f16_f32 v104, v94, v80
	v_add_f32_e32 v97, 1.0, v97
	v_log_f32_e32 v97, v97
	v_mov_b32_e32 v80, v66
	v_permlane32_swap_b32_e32 v102, v104
	v_add_f32_e32 v79, v79, v97
	v_cmp_lt_i32_e32 vcc, 57, v254
	s_nop 0
	s_nop 0
	v_cndmask_b32_e64 v97, 0, -v79, vcc
	v_fma_f32 v79, v81, s26, -v79
	v_cndmask_b32_e32 v247, v208, v79, vcc
	v_mul_f32_e32 v79, 0x3e0293ee, v98
	v_exp_f32_e64 v81, -|v79|
	v_max_f32_e32 v79, 0, v79
	v_add_f32_e32 v78, v97, v78
	v_cvt_pkrtz_f16_f32 v244, v96, v97
	v_add_f32_e32 v81, 1.0, v81
	v_log_f32_e32 v81, v81
	v_permlane32_swap_b32_e32 v242, v244
	v_add_f32_e32 v79, v79, v81
	v_cmp_lt_i32_e32 vcc, 26, v254
	s_nop 0
	s_nop 0
	v_cndmask_b32_e64 v81, 0, -v79, vcc
	v_fma_f32 v79, v98, s26, -v79
	v_cndmask_b32_e32 v248, v208, v79, vcc
	v_mul_f32_e32 v79, 0x3e0293ee, v82
	v_exp_f32_e64 v98, -|v79|
	v_max_f32_e32 v79, 0, v79
	v_add_f32_e32 v78, v81, v78
	v_add_f32_e32 v98, 1.0, v98
	v_log_f32_e32 v98, v98
	s_nop 0
	v_add_f32_e32 v79, v79, v98
	v_cmp_lt_i32_e32 vcc, 58, v254
	s_nop 0
	s_nop 0
	v_cndmask_b32_e64 v107, 0, -v79, vcc
	v_fma_f32 v79, v82, s26, -v79
	v_cndmask_b32_e32 v249, v208, v79, vcc
	v_mul_f32_e32 v79, 0x3e0293ee, v99
	v_exp_f32_e64 v82, -|v79|
	v_max_f32_e32 v79, 0, v79
	v_add_f32_e32 v78, v107, v78
	v_add_f32_e32 v82, 1.0, v82
	v_log_f32_e32 v82, v82
	s_nop 0
	v_add_f32_e32 v79, v79, v82
	v_cmp_lt_i32_e32 vcc, 27, v254
	s_nop 1
	v_cndmask_b32_e64 v82, 0, -v79, vcc
	v_fma_f32 v79, v99, s26, -v79
	v_cndmask_b32_e32 v250, v208, v79, vcc
	v_mul_f32_e32 v79, 0x3e0293ee, v83
	v_exp_f32_e64 v98, -|v79|
	v_max_f32_e32 v79, 0, v79
	v_cmp_lt_i32_e32 vcc, 59, v254
	v_add_f32_e32 v98, 1.0, v98
	v_log_f32_e32 v98, v98
	v_add_f32_e32 v78, v82, v78
	v_cvt_pkrtz_f16_f32 v99, v69, v70
	s_nop 1
	v_permlane32_swap_b32_e32 v99, v101
	v_add_f32_e32 v79, v79, v98
	v_cndmask_b32_e64 v67, 0, -v79, vcc
	v_fma_f32 v79, v83, s26, -v79
	v_cvt_pkrtz_f16_f32 v98, v100, v68
	v_cvt_pkrtz_f16_f32 v100, v71, v72
	v_cndmask_b32_e32 v251, v208, v79, vcc
	v_add_f32_e32 v252, v67, v78
	v_permlane32_swap_b32_e32 v98, v100
	v_cvt_pkrtz_f16_f32 v105, v81, v82
	v_cvt_pkrtz_f16_f32 v245, v107, v67
	v_mov_b32_e32 v67, v66
	v_mov_b32_e32 v68, v66
	v_mov_b32_e32 v69, v66
	v_mov_b32_e32 v70, v66
	v_mov_b32_e32 v71, v66
	v_mov_b32_e32 v72, v66
	v_mov_b32_e32 v78, v66
	v_mov_b32_e32 v79, v66
	v_mov_b32_e32 v81, v66
	v_permlane32_swap_b32_e32 v103, v105
	s_nop 0

; #define PG8_STAGEA(bufoff, h, ap, kb, go) do { if constexpr (GATHER) { PG8_STAGE(bufoff, (const char*)g.A + (kb), go[h]); } else { PG8_STAGE(bufoff, (ap) + (h) * hstep, voffA); } } while (0)
; #define PG8_WAIT_L(n) asm volatile("s_waitcnt lgkmcnt(" #n ")" ::: "memory")
; #define PG8_WAIT_V8R() do { if (relax) { if (GATHER && wid == 0 && has_next) asm volatile("s_waitcnt vmcnt(%0)" :: "n"(9 + Epi::NSTORES) : "memory"); else asm volatile("s_waitcnt vmcnt(%0)" :: "n"(8 + Epi::NSTORES) : "memory"); } else PG8_WAIT_V(8); } while (0)
; #define PG8_BAR __builtin_amdgcn_s_barrier()
; #define PG8_SCHED __builtin_amdgcn_sched_barrier(0)
; template <class Epi, class Sched, bool GATHER, bool FP8 = false>
; __device__ __forceinline__ void gemm_phase(LAS unsigned char* lds, LAS int* idx, const Gemm g, const Sched& S, const Epi& E) {
;     ...
;             const int relax = __builtin_amdgcn_readfirstlane(((t == 0) && (ui > 0)) ? 1 : 0);
;             PG8_LDB(B0, 0, 0); PG8_LDB(B1, 0, 1); PG8_SCHED; PG8_LDA(At, 0, 0); PG8_STAGEA(PG8_SA(1, 1), 1, a1, k1, gc);
;             PG8_WAIT_V8R(); PG8_WAIT_L(0); PG8_BAR; PG8_MMA(0, 0, At, B0); PG8_MMA(0, 1, At, B1); PG8_BAR; PG8_SCHED;
.LBB0_453:
	ds_read_b128 v[26:29], v226
	ds_read_b128 v[30:33], v227
	ds_read_b128 v[18:21], v228
	ds_read_b128 v[22:25], v229
	ds_read_b128 v[10:13], v231
	ds_read_b128 v[14:17], v232
	ds_read_b128 v[2:5], v233
	ds_read_b128 v[6:9], v234
	s_cmp_eq_u32 s64, 0
	s_cselect_b64 s[30:31], -1, 0
	s_and_b64 s[30:31], s[26:27], s[30:31]
	v_lshl_add_u64 v[214:215], v[210:211], 0, s[28:29]
	s_add_i32 m0, s39, 0xc000
	ds_read_b128 v[58:61], v244
	ds_read_b128 v[62:65], v244 offset:1024
	ds_read_b128 v[50:53], v244 offset:2048
	ds_read_b128 v[54:57], v244 offset:3072
	ds_read_b128 v[42:45], v244 offset:4096
	ds_read_b128 v[46:49], v244 offset:5120
	ds_read_b128 v[34:37], v244 offset:6144
	ds_read_b128 v[38:41], v244 offset:7168
	global_load_lds_dwordx4 v[214:215], off
	v_lshl_add_u64 v[214:215], v[212:213], 0, s[28:29]
	s_add_i32 m0, s39, 0xe000
	s_nop 0
	global_load_lds_dwordx4 v[214:215], off
	s_and_b64 vcc, exec, s[30:31]
	s_not_b64 s[34:35], s[30:31]
	s_mov_b64 s[30:31], -1
	s_cbranch_vccnz .LBB0_455
	s_waitcnt vmcnt(8)
	s_mov_b64 s[30:31], 0

; #define PG8_STAGEA(bufoff, h, ap, kb, go) do { if constexpr (GATHER) { PG8_STAGE(bufoff, (const char*)g.A + (kb), go[h]); } else { PG8_STAGE(bufoff, (ap) + (h) * hstep, voffA); } } while (0)
; #define PG8_WAIT_L(n) asm volatile("s_waitcnt lgkmcnt(" #n ")" ::: "memory")
; #define PG8_WAIT_V8R() do { if (relax) { if (GATHER && wid == 0 && has_next) asm volatile("s_waitcnt vmcnt(%0)" :: "n"(9 + Epi::NSTORES) : "memory"); else asm volatile("s_waitcnt vmcnt(%0)" :: "n"(8 + Epi::NSTORES) : "memory"); } else PG8_WAIT_V(8); } while (0)
; #define PG8_BAR __builtin_amdgcn_s_barrier()
; #define PG8_SCHED __builtin_amdgcn_sched_barrier(0)
; template <class Epi, class Sched, bool GATHER, bool FP8 = false>
; __device__ __forceinline__ void gemm_phase(LAS unsigned char* lds, LAS int* idx, const Gemm g, const Sched& S, const Epi& E) {
;     ...
;             const int relax = __builtin_amdgcn_readfirstlane(((t == 0) && (ui > 0)) ? 1 : 0);
;             PG8_LDB(B0, 0, 0); PG8_LDB(B1, 0, 1); PG8_SCHED; PG8_LDA(At, 0, 0); PG8_STAGEA(PG8_SA(1, 1), 1, a1, k1, gc);
;             PG8_WAIT_V8R(); PG8_WAIT_L(0); PG8_BAR; PG8_MMA(0, 0, At, B0); PG8_MMA(0, 1, At, B1); PG8_BAR; PG8_SCHED;
.LBB0_760:
	ds_read_b128 v[26:29], v203
	ds_read_b128 v[30:33], v205
	ds_read_b128 v[18:21], v207
	ds_read_b128 v[22:25], v233
	ds_read_b128 v[10:13], v234
	ds_read_b128 v[14:17], v235
	ds_read_b128 v[2:5], v236
	ds_read_b128 v[6:9], v237
	s_cmp_eq_u32 s23, 0
	s_cselect_b64 s[40:41], -1, 0
	s_and_b64 s[40:41], s[36:37], s[40:41]
	s_add_i32 m0, s54, 0xc000
	s_add_u32 s44, s14, s42
	s_addc_u32 s45, s15, s43
	ds_read_b128 v[58:61], v248
	ds_read_b128 v[62:65], v248 offset:1024
	ds_read_b128 v[50:53], v248 offset:2048
	ds_read_b128 v[54:57], v248 offset:3072
	ds_read_b128 v[42:45], v248 offset:4096
	ds_read_b128 v[46:49], v248 offset:5120
	ds_read_b128 v[34:37], v248 offset:6144
	ds_read_b128 v[38:41], v248 offset:7168
	global_load_lds_dwordx4 v202, s[44:45]
	s_add_i32 m0, s54, 0xe000
	s_nop 0
	global_load_lds_dwordx4 v206, s[44:45]
	s_and_b64 vcc, exec, s[40:41]
	s_not_b64 s[44:45], s[40:41]
	s_mov_b64 s[40:41], -1
	s_cbranch_vccnz .LBB0_762
	s_waitcnt vmcnt(8)
	s_mov_b64 s[40:41], 0

; #define PG8_STAGEA(bufoff, h, ap, kb, go) do { if constexpr (GATHER) { PG8_STAGE(bufoff, (const char*)g.A + (kb), go[h]); } else { PG8_STAGE(bufoff, (ap) + (h) * hstep, voffA); } } while (0)
; #define PG8_WAIT_L(n) asm volatile("s_waitcnt lgkmcnt(" #n ")" ::: "memory")
; #define PG8_WAIT_V8R() do { if (relax) { if (GATHER && wid == 0 && has_next) asm volatile("s_waitcnt vmcnt(%0)" :: "n"(9 + Epi::NSTORES) : "memory"); else asm volatile("s_waitcnt vmcnt(%0)" :: "n"(8 + Epi::NSTORES) : "memory"); } else PG8_WAIT_V(8); } while (0)
; #define PG8_BAR __builtin_amdgcn_s_barrier()
; #define PG8_SCHED __builtin_amdgcn_sched_barrier(0)
; template <class Epi, class Sched, bool GATHER, bool FP8 = false>
; __device__ __forceinline__ void gemm_phase(LAS unsigned char* lds, LAS int* idx, const Gemm g, const Sched& S, const Epi& E) {
;     ...
;             const int relax = __builtin_amdgcn_readfirstlane(((t == 0) && (ui > 0)) ? 1 : 0);
;             PG8_LDB(B0, 0, 0); PG8_LDB(B1, 0, 1); PG8_SCHED; PG8_LDA(At, 0, 0); PG8_STAGEA(PG8_SA(1, 1), 1, a1, k1, gc);
;             PG8_WAIT_V8R(); PG8_WAIT_L(0); PG8_BAR; PG8_MMA(0, 0, At, B0); PG8_MMA(0, 1, At, B1); PG8_BAR; PG8_SCHED;
.LBB0_858:
	ds_read_b128 v[26:29], v222
	ds_read_b128 v[30:33], v223
	ds_read_b128 v[18:21], v224
	ds_read_b128 v[22:25], v225
	ds_read_b128 v[10:13], v226
	ds_read_b128 v[14:17], v227
	ds_read_b128 v[2:5], v228
	ds_read_b128 v[6:9], v229
	s_cmp_eq_u32 s15, 0
	s_cselect_b64 s[26:27], -1, 0
	s_and_b64 s[26:27], s[22:23], s[26:27]
	v_lshl_add_u64 v[210:211], v[206:207], 0, s[24:25]
	s_add_i32 m0, s41, 0xc000
	ds_read_b128 v[58:61], v241
	ds_read_b128 v[62:65], v241 offset:1024
	ds_read_b128 v[50:53], v241 offset:2048
	ds_read_b128 v[54:57], v241 offset:3072
	ds_read_b128 v[42:45], v241 offset:4096
	ds_read_b128 v[46:49], v241 offset:5120
	ds_read_b128 v[34:37], v241 offset:6144
	ds_read_b128 v[38:41], v241 offset:7168
	global_load_lds_dwordx4 v[210:211], off
	v_lshl_add_u64 v[210:211], v[208:209], 0, s[24:25]
	s_add_i32 m0, s41, 0xe000
	s_nop 0
	global_load_lds_dwordx4 v[210:211], off
	s_and_b64 vcc, exec, s[26:27]
	s_not_b64 s[28:29], s[26:27]
	s_mov_b64 s[26:27], -1
	s_cbranch_vccnz .LBB0_860
	s_waitcnt vmcnt(8)
	s_mov_b64 s[26:27], 0

; #define PG8_STAGEA(bufoff, h, ap, kb, go) do { if constexpr (GATHER) { PG8_STAGE(bufoff, (const char*)g.A + (kb), go[h]); } else { PG8_STAGE(bufoff, (ap) + (h) * hstep, voffA); } } while (0)
; #define PG8_WAIT_L(n) asm volatile("s_waitcnt lgkmcnt(" #n ")" ::: "memory")
; #define PG8_WAIT_V8R() do { if (relax) { if (GATHER && wid == 0 && has_next) asm volatile("s_waitcnt vmcnt(%0)" :: "n"(9 + Epi::NSTORES) : "memory"); else asm volatile("s_waitcnt vmcnt(%0)" :: "n"(8 + Epi::NSTORES) : "memory"); } else PG8_WAIT_V(8); } while (0)
; #define PG8_BAR __builtin_amdgcn_s_barrier()
; #define PG8_SCHED __builtin_amdgcn_sched_barrier(0)
; template <class Epi, class Sched, bool GATHER, bool FP8 = false>
; __device__ __forceinline__ void gemm_phase(LAS unsigned char* lds, LAS int* idx, const Gemm g, const Sched& S, const Epi& E) {
;     ...
;             const int relax = __builtin_amdgcn_readfirstlane(((t == 0) && (ui > 0)) ? 1 : 0);
;             PG8_LDB(B0, 0, 0); PG8_LDB(B1, 0, 1); PG8_SCHED; PG8_LDA(At, 0, 0); PG8_STAGEA(PG8_SA(1, 1), 1, a1, k1, gc);
;             PG8_WAIT_V8R(); PG8_WAIT_L(0); PG8_BAR; PG8_MMA(0, 0, At, B0); PG8_MMA(0, 1, At, B1); PG8_BAR; PG8_SCHED;
.LBB0_1014:
	ds_read_b128 v[26:29], v228
	ds_read_b128 v[30:33], v229
	ds_read_b128 v[18:21], v232
	ds_read_b128 v[22:25], v233
	ds_read_b128 v[10:13], v234
	ds_read_b128 v[14:17], v235
	ds_read_b128 v[2:5], v236
	ds_read_b128 v[6:9], v237
	s_cmp_eq_u32 s68, 0
	s_cselect_b64 s[26:27], -1, 0
	s_and_b64 s[26:27], s[8:9], s[26:27]
	v_lshl_add_u64 v[216:217], v[212:213], 0, s[24:25]
	s_add_i32 m0, s38, 0xc000
	ds_read_b128 v[58:61], v247
	ds_read_b128 v[62:65], v247 offset:1024
	ds_read_b128 v[50:53], v247 offset:2048
	ds_read_b128 v[54:57], v247 offset:3072
	ds_read_b128 v[42:45], v247 offset:4096
	ds_read_b128 v[46:49], v247 offset:5120
	ds_read_b128 v[34:37], v247 offset:6144
	ds_read_b128 v[38:41], v247 offset:7168
	global_load_lds_dwordx4 v[216:217], off
	v_lshl_add_u64 v[216:217], v[214:215], 0, s[24:25]
	s_add_i32 m0, s38, 0xe000
	s_nop 0
	global_load_lds_dwordx4 v[216:217], off
	s_and_b64 vcc, exec, s[26:27]
	s_not_b64 s[28:29], s[26:27]
	s_mov_b64 s[26:27], -1
	s_cbranch_vccnz .LBB0_1016
	s_waitcnt vmcnt(8)
	s_mov_b64 s[26:27], 0

; #define PG8_STAGEA(bufoff, h, ap, kb, go) do { if constexpr (GATHER) { PG8_STAGE(bufoff, (const char*)g.A + (kb), go[h]); } else { PG8_STAGE(bufoff, (ap) + (h) * hstep, voffA); } } while (0)
; #define PG8_WAIT_L(n) asm volatile("s_waitcnt lgkmcnt(" #n ")" ::: "memory")
; #define PG8_WAIT_V8R() do { if (relax) { if (GATHER && wid == 0 && has_next) asm volatile("s_waitcnt vmcnt(%0)" :: "n"(9 + Epi::NSTORES) : "memory"); else asm volatile("s_waitcnt vmcnt(%0)" :: "n"(8 + Epi::NSTORES) : "memory"); } else PG8_WAIT_V(8); } while (0)
; #define PG8_BAR __builtin_amdgcn_s_barrier()
; #define PG8_SCHED __builtin_amdgcn_sched_barrier(0)
; template <class Epi, class Sched, bool GATHER, bool FP8 = false>
; __device__ __forceinline__ void gemm_phase(LAS unsigned char* lds, LAS int* idx, const Gemm g, const Sched& S, const Epi& E) {
;     ...
;             const int relax = __builtin_amdgcn_readfirstlane(((t == 0) && (ui > 0)) ? 1 : 0);
;             PG8_LDB(B0, 0, 0); PG8_LDB(B1, 0, 1); PG8_SCHED; PG8_LDA(At, 0, 0); PG8_STAGEA(PG8_SA(1, 1), 1, a1, k1, gc);
;             PG8_WAIT_V8R(); PG8_WAIT_L(0); PG8_BAR; PG8_MMA(0, 0, At, B0); PG8_MMA(0, 1, At, B1); PG8_BAR; PG8_SCHED;
.LBB0_1226:
	ds_read_b128 v[26:29], v226
	ds_read_b128 v[30:33], v227
	ds_read_b128 v[18:21], v228
	ds_read_b128 v[22:25], v229
	ds_read_b128 v[10:13], v232
	ds_read_b128 v[14:17], v233
	ds_read_b128 v[2:5], v234
	ds_read_b128 v[6:9], v235
	s_cmp_eq_u32 s64, 0
	s_cselect_b64 s[30:31], -1, 0
	s_and_b64 s[30:31], s[26:27], s[30:31]
	v_lshl_add_u64 v[214:215], v[210:211], 0, s[28:29]
	s_add_i32 m0, s39, 0xc000
	ds_read_b128 v[58:61], v245
	ds_read_b128 v[62:65], v245 offset:1024
	ds_read_b128 v[50:53], v245 offset:2048
	ds_read_b128 v[54:57], v245 offset:3072
	ds_read_b128 v[42:45], v245 offset:4096
	ds_read_b128 v[46:49], v245 offset:5120
	ds_read_b128 v[34:37], v245 offset:6144
	ds_read_b128 v[38:41], v245 offset:7168
	global_load_lds_dwordx4 v[214:215], off
	v_lshl_add_u64 v[214:215], v[212:213], 0, s[28:29]
	s_add_i32 m0, s39, 0xe000
	s_nop 0
	global_load_lds_dwordx4 v[214:215], off
	s_and_b64 vcc, exec, s[30:31]
	s_not_b64 s[34:35], s[30:31]
	s_mov_b64 s[30:31], -1
	s_cbranch_vccnz .LBB0_1228
	s_waitcnt vmcnt(8)
	s_mov_b64 s[30:31], 0

; #define PG8_STAGEA(bufoff, h, ap, kb, go) do { if constexpr (GATHER) { PG8_STAGE(bufoff, (const char*)g.A + (kb), go[h]); } else { PG8_STAGE(bufoff, (ap) + (h) * hstep, voffA); } } while (0)
; #define PG8_WAIT_L(n) asm volatile("s_waitcnt lgkmcnt(" #n ")" ::: "memory")
; #define PG8_WAIT_V8R() do { if (relax) { if (GATHER && wid == 0 && has_next) asm volatile("s_waitcnt vmcnt(%0)" :: "n"(9 + Epi::NSTORES) : "memory"); else asm volatile("s_waitcnt vmcnt(%0)" :: "n"(8 + Epi::NSTORES) : "memory"); } else PG8_WAIT_V(8); } while (0)
; #define PG8_BAR __builtin_amdgcn_s_barrier()
; #define PG8_SCHED __builtin_amdgcn_sched_barrier(0)
; template <class Epi, class Sched, bool GATHER, bool FP8 = false>
; __device__ __forceinline__ void gemm_phase(LAS unsigned char* lds, LAS int* idx, const Gemm g, const Sched& S, const Epi& E) {
;     ...
;             const int relax = __builtin_amdgcn_readfirstlane(((t == 0) && (ui > 0)) ? 1 : 0);
;             PG8_LDB(B0, 0, 0); PG8_LDB(B1, 0, 1); PG8_SCHED; PG8_LDA(At, 0, 0); PG8_STAGEA(PG8_SA(1, 1), 1, a1, k1, gc);
;             PG8_WAIT_V8R(); PG8_WAIT_L(0); PG8_BAR; PG8_MMA(0, 0, At, B0); PG8_MMA(0, 1, At, B1); PG8_BAR; PG8_SCHED;
.LBB0_1533:
	ds_read_b128 v[26:29], v203
	ds_read_b128 v[30:33], v205
	ds_read_b128 v[18:21], v207
	ds_read_b128 v[22:25], v232
	ds_read_b128 v[10:13], v233
	ds_read_b128 v[14:17], v234
	ds_read_b128 v[2:5], v235
	ds_read_b128 v[6:9], v236
	s_cmp_eq_u32 s23, 0
	s_cselect_b64 s[40:41], -1, 0
	s_and_b64 s[40:41], s[36:37], s[40:41]
	s_add_i32 m0, s52, 0xc000
	s_add_u32 s44, s14, s42
	s_addc_u32 s45, s15, s43
	ds_read_b128 v[58:61], v247
	ds_read_b128 v[62:65], v247 offset:1024
	ds_read_b128 v[50:53], v247 offset:2048
	ds_read_b128 v[54:57], v247 offset:3072
	ds_read_b128 v[42:45], v247 offset:4096
	ds_read_b128 v[46:49], v247 offset:5120
	ds_read_b128 v[34:37], v247 offset:6144
	ds_read_b128 v[38:41], v247 offset:7168
	global_load_lds_dwordx4 v202, s[44:45]
	s_add_i32 m0, s52, 0xe000
	s_nop 0
	global_load_lds_dwordx4 v206, s[44:45]
	s_and_b64 vcc, exec, s[40:41]
	s_not_b64 s[44:45], s[40:41]
	s_mov_b64 s[40:41], -1
	s_cbranch_vccnz .LBB0_1535
	s_waitcnt vmcnt(8)
	s_mov_b64 s[40:41], 0

; #define PG8_STAGEA(bufoff, h, ap, kb, go) do { if constexpr (GATHER) { PG8_STAGE(bufoff, (const char*)g.A + (kb), go[h]); } else { PG8_STAGE(bufoff, (ap) + (h) * hstep, voffA); } } while (0)
; #define PG8_WAIT_L(n) asm volatile("s_waitcnt lgkmcnt(" #n ")" ::: "memory")
; #define PG8_WAIT_V8R() do { if (relax) { if (GATHER && wid == 0 && has_next) asm volatile("s_waitcnt vmcnt(%0)" :: "n"(9 + Epi::NSTORES) : "memory"); else asm volatile("s_waitcnt vmcnt(%0)" :: "n"(8 + Epi::NSTORES) : "memory"); } else PG8_WAIT_V(8); } while (0)
; #define PG8_BAR __builtin_amdgcn_s_barrier()
; #define PG8_SCHED __builtin_amdgcn_sched_barrier(0)
; template <class Epi, class Sched, bool GATHER, bool FP8 = false>
; __device__ __forceinline__ void gemm_phase(LAS unsigned char* lds, LAS int* idx, const Gemm g, const Sched& S, const Epi& E) {
;     ...
;             const int relax = __builtin_amdgcn_readfirstlane(((t == 0) && (ui > 0)) ? 1 : 0);
;             PG8_LDB(B0, 0, 0); PG8_LDB(B1, 0, 1); PG8_SCHED; PG8_LDA(At, 0, 0); PG8_STAGEA(PG8_SA(1, 1), 1, a1, k1, gc);
;             PG8_WAIT_V8R(); PG8_WAIT_L(0); PG8_BAR; PG8_MMA(0, 0, At, B0); PG8_MMA(0, 1, At, B1); PG8_BAR; PG8_SCHED;
.LBB0_1631:
	ds_read_b128 v[24:27], v221
	ds_read_b128 v[28:31], v222
	ds_read_b128 v[16:19], v223
	ds_read_b128 v[20:23], v224
	ds_read_b128 v[8:11], v225
	ds_read_b128 v[12:15], v226
	ds_read_b128 v[0:3], v227
	ds_read_b128 v[4:7], v228
	s_cmp_eq_u32 s15, 0
	s_cselect_b64 s[26:27], -1, 0
	s_and_b64 s[26:27], s[22:23], s[26:27]
	v_lshl_add_u64 v[208:209], v[204:205], 0, s[24:25]
	s_add_i32 m0, s40, 0xc000
	ds_read_b128 v[56:59], v239
	ds_read_b128 v[60:63], v239 offset:1024
	ds_read_b128 v[48:51], v239 offset:2048
	ds_read_b128 v[52:55], v239 offset:3072
	ds_read_b128 v[40:43], v239 offset:4096
	ds_read_b128 v[44:47], v239 offset:5120
	ds_read_b128 v[32:35], v239 offset:6144
	ds_read_b128 v[36:39], v239 offset:7168
	global_load_lds_dwordx4 v[208:209], off
	v_lshl_add_u64 v[208:209], v[206:207], 0, s[24:25]
	s_add_i32 m0, s40, 0xe000
	s_nop 0
	global_load_lds_dwordx4 v[208:209], off
	s_and_b64 vcc, exec, s[26:27]
	s_not_b64 s[28:29], s[26:27]
	s_mov_b64 s[26:27], -1
	s_cbranch_vccnz .LBB0_1633
	s_waitcnt vmcnt(8)
	s_mov_b64 s[26:27], 0
